# grid barrier: status words read back to back; the workgroup that sets the per-CU flag does not wait for that store before the workgroup barrier
# speedup vs baseline: 1.0121x; 1.0061x over previous
; __device__ __forceinline__ void xcd_barrier(const XcdBarrier& b) {
;     asm volatile("s_waitcnt vmcnt(0)" ::: "memory");
;     __syncthreads();
;     if (threadIdx.x == 0) {
;         unsigned* bar = b.bar;
;         __builtin_amdgcn_s_waitcnt(0);
;         unsigned nloc = b.st[0], nx = b.st[1];
.LBB0_710:
	s_waitcnt vmcnt(0)
	s_waitcnt lgkmcnt(0)
	s_barrier
	s_mov_b64 s[4:5], exec
	v_readlane_b32 s6, v253, 3
	v_readlane_b32 s7, v253, 4
	s_and_b64 s[6:7], s[4:5], s[6:7]
	s_mov_b64 exec, s[6:7]
	s_cbranch_execnz .LBB0_711
.Lxb_to11:
	s_getpc_b64 s[98:99]

; __device__ __forceinline__ void xcd_barrier(const XcdBarrier& b) {
;     ...
;     if (threadIdx.x == 0) {
;         unsigned* bar = b.bar;
;         __builtin_amdgcn_s_waitcnt(0);
;         unsigned nloc = b.st[0], nx = b.st[1];
;         if (nloc == 0u) { xcd_barrier_complete(bar, b.x, nloc, nx); b.st[0] = nloc; b.st[1] = nx; }
.LBB0_711:
	s_mov_b64 s[6:7], src_shared_base
	v_mov_b32_e32 v153, s7
	s_waitcnt vmcnt(0) expcnt(0) lgkmcnt(0)
	flat_load_dword v4, v[152:153] sc0 sc1
	v_mov_b32_e32 v155, s7
	flat_load_dword v2, v[154:155] sc0 sc1
	s_waitcnt vmcnt(0) lgkmcnt(0)
	v_cmp_eq_u32_e32 vcc, 0, v4
	s_and_saveexec_b64 s[28:29], vcc
	s_cbranch_execz .LBB0_726
	v_readlane_b32 s16, v253, 1
	v_readlane_b32 s17, v253, 2
	s_load_dwordx2 s[6:7], s[16:17], 0x4
	s_mov_b32 s16, 1
	s_waitcnt lgkmcnt(0)
	s_mul_i32 s15, s6, s3
	s_mul_i32 s15, s15, s7
	s_branch .LBB0_714
